# moe_stagger 4 groups x 1.5us (chain of 4 instead of 8)
# baseline (speedup 1.0000x reference)
.LBB0_1847:
	s_or_b64 exec, exec, s[0:1]
	v_readlane_b32 s0, v254, 4
	s_mov_b32 s2, 0
	s_mov_b32 s4, s0
	v_readlane_b32 s54, v254, 2
	v_readlane_b32 s0, v254, 3
	s_waitcnt lgkmcnt(0)
	s_barrier
	s_lshr_b32 s98, s4, 3
	s_and_b32 s98, s98, 3
	s_cmp_eq_u32 s98, 0
	s_cbranch_scc1 .Lstg_done
